# combined version plus prep set-up load batching (norm1 hoisting dropped)
# speedup vs baseline: 1.0183x; 1.0183x over previous
.LBB0_307:
	s_or_b64 exec, exec, s[24:25]
	v_readlane_b32 s8, v254, 7
	s_mov_b32 s4, s61
	s_mov_b32 s22, s61
	v_readlane_b32 s0, v254, 3
	v_readlane_b32 s9, v254, 8
	s_waitcnt lgkmcnt(0)
	s_barrier
	v_mbcnt_lo_u32_b32 v33, -1, 0
	v_mbcnt_hi_u32_b32 v33, -1, v33
	s_load_dword s1, s[8:9], 0xb0
	s_cmpk_gt_i32 s0, 0x3ff
	s_waitcnt lgkmcnt(0)
	s_cbranch_scc1 .LBB0_324
	s_load_dwordx2 s[6:7], s[8:9], 0xa8
	s_movk_i32 s2, 0x48
	v_readlane_b32 s24, v254, 55
	v_readlane_b32 s25, v254, 56
	v_and_b32_e32 v36, 15, v33
	s_waitcnt lgkmcnt(0)
	s_add_u32 s10, s6, 0x54000000
	s_addc_u32 s11, s7, 0
	s_add_u32 s12, s6, 0x1800000
	s_addc_u32 s13, s7, 0
	s_cmp_gt_u32 s22, 3
	s_cselect_b64 s[14:15], -1, 0
	s_cmp_lt_u32 s22, 4
	s_cselect_b32 s2, s2, 0x50
	s_add_u32 s2, s8, s2
	s_addc_u32 s3, s9, 0
	s_load_dwordx2 s[2:3], s[2:3], 0x0
	s_lshl_b32 s40, s24, 13
	s_lshl_b64 s[16:17], s[40:41], 2
	v_bfe_u32 v35, v33, 4, 2
	v_lshl_or_b32 v37, s4, 6, v33
	s_waitcnt lgkmcnt(0)
	s_add_u32 s2, s2, s16
	s_addc_u32 s3, s3, s17
	s_add_u32 s16, s6, 0xe00000
	s_addc_u32 s17, s7, 0
	s_lshl_b32 s25, s22, 4
	s_and_b32 s23, s25, 16
	v_or_b32_e32 v0, s23, v36
	v_lshlrev_b32_e32 v0, 2, v0
	v_lshl_or_b32 v31, v35, 11, v0
	v_or_b32_e32 v178, 0x6000, v31
	global_load_dword v114, v178, s[2:3] offset:128
	v_or_b32_e32 v179, 0x6100, v31
	global_load_dword v115, v179, s[2:3] offset:128
	v_or_b32_e32 v180, 0x6300, v31
	global_load_dword v116, v180, s[2:3] offset:128
	v_or_b32_e32 v181, 0x6700, v31
	global_load_dword v117, v181, s[2:3] offset:128
	v_or_b32_e32 v178, 0x4700, v31
	global_load_dword v118, v178, s[2:3] offset:128
	v_or_b32_e32 v179, 0x100, v31
	global_load_dword v119, v179, s[2:3] offset:128
	v_or_b32_e32 v180, 0x300, v31
	global_load_dword v120, v180, s[2:3] offset:128
	v_or_b32_e32 v181, 0x6500, v31
	global_load_dword v121, v181, s[2:3] offset:128
	v_or_b32_e32 v178, 0x4300, v31
	global_load_dword v122, v178, s[2:3] offset:128
	v_or_b32_e32 v179, 0x2700, v31
	global_load_dword v123, v179, s[2:3] offset:128
	v_or_b32_e32 v180, 0x4100, v31
	global_load_dword v124, v180, s[2:3] offset:128
	v_or_b32_e32 v181, 0x2300, v31
	global_load_dword v125, v181, s[2:3] offset:128
	v_or_b32_e32 v178, 0x4500, v31
	global_load_dword v126, v178, s[2:3] offset:128
	v_or_b32_e32 v179, 0x2100, v31
	global_load_dword v127, v179, s[2:3] offset:128
	v_or_b32_e32 v180, 0x2500, v31
	global_load_dword v128, v180, s[2:3] offset:128
	v_or_b32_e32 v181, 0x6200, v31
	global_load_dword v129, v181, s[2:3] offset:128
	v_or_b32_e32 v178, 0x6400, v31
	global_load_dword v130, v178, s[2:3] offset:128
	v_or_b32_e32 v179, 0x6600, v31
	global_load_dword v131, v179, s[2:3] offset:128
	v_or_b32_e32 v180, 0x4000, v31
	global_load_dword v132, v180, s[2:3] offset:128
	v_or_b32_e32 v181, 0x4200, v31
	global_load_dword v133, v181, s[2:3] offset:128
	v_or_b32_e32 v178, 0x4400, v31
	global_load_dword v134, v178, s[2:3] offset:128
	v_or_b32_e32 v179, 0x4600, v31
	global_load_dword v135, v179, s[2:3] offset:128
	v_or_b32_e32 v180, 0x2000, v31
	global_load_dword v136, v180, s[2:3] offset:128
	v_or_b32_e32 v181, 0x2200, v31
	global_load_dword v137, v181, s[2:3] offset:128
	v_or_b32_e32 v178, 0x2400, v31
	global_load_dword v138, v178, s[2:3] offset:128
	v_or_b32_e32 v179, 0x2600, v31
	global_load_dword v139, v179, s[2:3] offset:128
	global_load_dword v140, v31, s[2:3] offset:128
	v_or_b32_e32 v181, 0x200, v31
	global_load_dword v141, v181, s[2:3] offset:128
	v_or_b32_e32 v178, 0x500, v31
	global_load_dword v142, v178, s[2:3] offset:128
	v_or_b32_e32 v179, 0x400, v31
	global_load_dword v143, v179, s[2:3] offset:128
	v_or_b32_e32 v180, 0x700, v31
	global_load_dword v144, v180, s[2:3] offset:128
	v_or_b32_e32 v181, 0x600, v31
	global_load_dword v145, v181, s[2:3] offset:128
	v_or_b32_e32 v178, 0x6000, v31
	global_load_dword v146, v178, s[2:3]
	v_or_b32_e32 v179, 0x6100, v31
	global_load_dword v147, v179, s[2:3]
	v_or_b32_e32 v180, 0x6200, v31
	global_load_dword v148, v180, s[2:3]
	v_or_b32_e32 v181, 0x6300, v31
	global_load_dword v149, v181, s[2:3]
	v_or_b32_e32 v178, 0x6400, v31
	global_load_dword v150, v178, s[2:3]
	v_or_b32_e32 v179, 0x6500, v31
	global_load_dword v151, v179, s[2:3]
	v_or_b32_e32 v180, 0x6600, v31
	global_load_dword v152, v180, s[2:3]
	v_or_b32_e32 v181, 0x6700, v31
	global_load_dword v153, v181, s[2:3]
	v_or_b32_e32 v178, 0x4000, v31
	global_load_dword v154, v178, s[2:3]
	v_or_b32_e32 v179, 0x4100, v31
	global_load_dword v155, v179, s[2:3]
	v_or_b32_e32 v180, 0x4200, v31
	global_load_dword v156, v180, s[2:3]
	v_or_b32_e32 v181, 0x4300, v31
	global_load_dword v157, v181, s[2:3]
	v_or_b32_e32 v178, 0x4400, v31
	global_load_dword v158, v178, s[2:3]
	v_or_b32_e32 v179, 0x4500, v31
	global_load_dword v159, v179, s[2:3]
	v_or_b32_e32 v180, 0x4600, v31
	global_load_dword v160, v180, s[2:3]
	v_or_b32_e32 v181, 0x4700, v31
	global_load_dword v161, v181, s[2:3]
	v_or_b32_e32 v178, 0x2000, v31
	global_load_dword v162, v178, s[2:3]
	v_or_b32_e32 v179, 0x2100, v31
	global_load_dword v163, v179, s[2:3]
	v_or_b32_e32 v180, 0x2200, v31
	global_load_dword v164, v180, s[2:3]
	v_or_b32_e32 v181, 0x2300, v31
	global_load_dword v165, v181, s[2:3]
	v_or_b32_e32 v178, 0x2400, v31
	global_load_dword v166, v178, s[2:3]
	v_or_b32_e32 v179, 0x2500, v31
	global_load_dword v167, v179, s[2:3]
	v_or_b32_e32 v180, 0x2600, v31
	global_load_dword v168, v180, s[2:3]
	v_or_b32_e32 v181, 0x2700, v31
	global_load_dword v169, v181, s[2:3]
	global_load_dword v170, v31, s[2:3]
	global_load_dword v171, v31, s[2:3] offset:256
	global_load_dword v172, v31, s[2:3] offset:512
	global_load_dword v173, v31, s[2:3] offset:768
	global_load_dword v174, v31, s[2:3] offset:1024
	global_load_dword v175, v31, s[2:3] offset:1280
	global_load_dword v176, v31, s[2:3] offset:1536
	global_load_dword v177, v31, s[2:3] offset:1792
	s_add_u32 s18, s6, 0x440000
	s_addc_u32 s19, s7, 0
	s_add_u32 s20, s6, 0x400000
	s_addc_u32 s21, s7, 0
	s_lshl_b32 s40, s24, 7
	s_lshl_b64 s[4:5], s[40:41], 2
	v_and_b32_e32 v34, 63, v33
	v_ashrrev_i32_e32 v96, 3, v37
	v_and_b32_e32 v37, 7, v33
	v_and_or_b32 v97, s25, 32, v36
	v_lshl_or_b32 v36, v35, 2, s23
	v_lshlrev_b32_e32 v32, 1, v34
	v_lshlrev_b32_e32 v184, 4, v37
	v_mov_b32_e32 v35, v185
	v_lshl_add_u64 v[68:69], s[18:19], 0, v[184:185]
	v_lshl_add_u64 v[66:67], s[20:21], 0, v[184:185]
	v_or_b32_e32 v99, 16, v97
	v_lshlrev_b32_e32 v84, 1, v32
	v_lshlrev_b32_e32 v39, 3, v33
	v_and_b32_e32 v40, 8, v39
	v_lshl_add_u32 v39, v34, 2, 0
	v_and_b32_e32 v33, 48, v33
	v_add_u32_e32 v33, 0, v33
	v_lshlrev_b32_e32 v82, 1, v40
	v_lshlrev_b32_e32 v42, 2, v40
	v_lshl_add_u32 v41, v97, 1, 0
	v_mov_b32_e32 v43, v185
	v_lshl_add_u64 v[42:43], s[6:7], 0, v[42:43]
	s_load_dwordx2 s[2:3], s[8:9], 0x40
	s_waitcnt lgkmcnt(0)
	s_add_u32 s2, s2, s4
	s_addc_u32 s3, s3, s5
	v_cmp_eq_u32_e64 s[4:5], 2, v37
	s_lshl_b32 s40, s24, 2
	s_lshl_b32 s24, s22, 3
	s_mulk_i32 s22, 0x880
	s_lshl_b32 s25, s0, 6
	s_lshl_b32 s26, s1, 6
	v_add_u32_e32 v100, s22, v39
	s_waitcnt vmcnt(0)
	v_cvt_pk_bf16_f32 v0, v114, v115
	v_cvt_pk_bf16_f32 v1, v129, v116
	v_cvt_pk_bf16_f32 v2, v130, v121
	v_cvt_pk_bf16_f32 v3, v131, v117
	v_cvt_pk_bf16_f32 v4, v132, v124
	v_cvt_pk_bf16_f32 v5, v133, v122
	v_cvt_pk_bf16_f32 v6, v134, v126
	v_cvt_pk_bf16_f32 v7, v135, v118
	v_cvt_pk_bf16_f32 v8, v136, v127
	v_cvt_pk_bf16_f32 v9, v137, v125
	v_cvt_pk_bf16_f32 v10, v138, v128
	v_cvt_pk_bf16_f32 v11, v139, v123
	v_cvt_pk_bf16_f32 v12, v140, v119
	v_cvt_pk_bf16_f32 v13, v141, v120
	v_cvt_pk_bf16_f32 v14, v143, v142
	v_cvt_pk_bf16_f32 v15, v145, v144
	v_cvt_pk_bf16_f32 v16, v146, v147
	v_cvt_pk_bf16_f32 v17, v148, v149
	v_cvt_pk_bf16_f32 v18, v150, v151
	v_cvt_pk_bf16_f32 v19, v152, v153
	v_cvt_pk_bf16_f32 v20, v154, v155
	v_cvt_pk_bf16_f32 v21, v156, v157
	v_cvt_pk_bf16_f32 v22, v158, v159
	v_cvt_pk_bf16_f32 v23, v160, v161
	v_cvt_pk_bf16_f32 v24, v162, v163
	v_cvt_pk_bf16_f32 v25, v164, v165
	v_cvt_pk_bf16_f32 v26, v166, v167
	v_cvt_pk_bf16_f32 v27, v168, v169
	v_cvt_pk_bf16_f32 v28, v170, v171
	v_cvt_pk_bf16_f32 v29, v172, v173
	v_cvt_pk_bf16_f32 v30, v174, v175
	v_cvt_pk_bf16_f32 v31, v176, v177
	v_lshlrev_b32_e32 v38, 3, v34
	global_load_dwordx2 v[64:65], v38, s[2:3]
	v_lshlrev_b32_e32 v34, 2, v36
	s_mov_b64 s[2:3], 0x480000
	v_lshl_add_u64 v[76:77], s[18:19], 0, v[34:35]
	s_movk_i32 s18, 0x90
	v_lshl_add_u64 v[70:71], v[42:43], 0, s[2:3]
	s_mov_b64 s[2:3], 0x4a0000
	v_lshl_add_u64 v[74:75], s[20:21], 0, v[34:35]
	v_mul_lo_u32 v35, v96, s18
	v_lshl_add_u64 v[72:73], v[42:43], 0, s[2:3]
	v_and_b32_e32 v42, 0x60, v184
	v_add3_u32 v98, 0, v35, v184
	v_lshlrev_b32_e32 v184, 1, v36
	v_lshlrev_b32_e32 v38, 2, v37
	v_cmp_gt_u32_e64 s[2:3], 2, v37
	v_lshlrev_b32_e32 v34, 3, v37
	v_mul_u32_u24_e32 v35, 0x110, v97
	v_mul_u32_u24_e32 v43, 0x90, v36
	v_lshl_add_u64 v[36:37], s[6:7], 0, v[184:185]
	s_mov_b64 s[6:7], 0x1000000
	v_lshl_add_u64 v[78:79], v[36:37], 0, s[6:7]
	v_lshlrev_b32_e32 v184, 1, v38
	v_lshlrev_b32_e32 v80, 1, v42
	s_lshl_b64 s[18:19], s[40:41], 2
	v_add_u32_e32 v101, v33, v35
	v_lshlrev_b32_e32 v86, 1, v34
	v_add_u32_e32 v102, v41, v43
	s_branch .LBB0_310
